# MoBA unit set-up: Q fragments and K/V tiles 0-2 requested before the gating pass; block-mean table fill in one round trip
# speedup vs baseline: 1.0061x; 1.0061x over previous
; __device__ __forceinline__ void moba_unit(Frame& F, const AttnBufs& A, int b, int h, int qb) {
;     ...
;     for (int i = tid; i < 1024; i += 512) { const int j = i >> 6, d = i & 63; float v = 0.f;
;         if (j < qb) { const float* p = A.KMP + ((size_t)((b * 16 + j) * 4 + h) * 2) * 64 + d; v = p[0] + p[64]; } KM[i] = v; }
.LBB0_278:
	s_and_b64 s[8:9], s[4:5], exec
	v_readlane_b32 s8, v254, 31
	v_readlane_b32 s9, v254, 33
	s_cselect_b32 s20, s8, s9
	s_and_saveexec_b64 s[8:9], s[0:1]
	s_cbranch_execz .LBB0_283
	v_ashrrev_i32_e32 v5, 6, v232
	v_lshl_add_u32 v4, v5, 2, s21
	v_add_u32_e32 v6, 32, v4
	v_cmp_gt_i32_e32 vcc, s20, v5
	v_add_u32_e32 v3, 8, v5
	v_cmp_gt_i32_e64 s[10:11], s20, v3
	v_ashrrev_i32_e32 v5, 31, v4
	v_ashrrev_i32_e32 v7, 31, v6
	v_lshlrev_b64 v[4:5], 9, v[4:5]
	v_lshlrev_b64 v[6:7], 9, v[6:7]
	v_lshl_add_u64 v[4:5], v[158:159], 0, v[4:5]
	v_lshl_add_u64 v[6:7], v[158:159], 0, v[6:7]
	flat_load_dword v8, v[4:5]
	flat_load_dword v9, v[4:5] offset:256
	flat_load_dword v10, v[6:7]
	flat_load_dword v11, v[6:7] offset:256
	s_waitcnt vmcnt(0) lgkmcnt(0)
	v_add_f32_e32 v8, v8, v9
	v_add_f32_e32 v10, v10, v11
	v_cndmask_b32_e32 v8, 0, v8, vcc
	v_cndmask_b32_e64 v10, 0, v10, s[10:11]
	ds_write_b32 v161, v8
	ds_write_b32 v161, v10 offset:2048
